# all weight conversions for layers 1-3 moved into GEMM-tail workgroups (UP1 next-layer in P3 tail, small matrices in P13 tail); P0 and its seam skipped for layers 1-3
# speedup vs baseline: 1.0039x; 1.0039x over previous
; #define LAS __attribute__((address_space(3)))
; #define IN(k) in_range(lo, hi, (k))
; __global__ void __launch_bounds__(NWAVES * 64, 2) mk_fwd(Args args) {
;     ...
;     for (int l = 0; l < DEPTH; ++l) {
;         const int pb = 1 + l * NPH;
;         if (hi <= pb || lo >= pb + NPH) continue;
;         if (EN(0) && IN(pb + 0)) {
;             PH_LOCALS
;             LAS float* scr = (LAS float*)(lds + RING_OFF + wave * 16640);   static_assert(8 * 16640 <= LDSCTL_OFF, "converter scratch below the LDS control words");
;             constexpr int I_UP = (D / 64) * (NUP / 64), I_DN = (DFF / 64) * (D / 64), I_IN = (D / 64) * (DINP / 64), I_GLU = 16 * 16, I_L = 4 * 16, I_V1 = 16 * 4, I_V2 = 4 * 16,
;                           I_BS5 = 16 * 32, I_BAT = 8 * 32, I_BRW = 16 * 32, I_OUT = 32 * 32;
;             constexpr int NITEMS = 2 * I_UP + 2 * I_DN + I_IN + I_GLU + 3 * I_L + I_V1 + I_V2 + I_BS5 + I_BAT + I_BRW + I_OUT;
;             const int lv = l > 0 ? l - 1 : 0;
;     ...
;             for (int it = gw; it < NITEMS; it += NGW) {
;                 ConvItem ca; CONV_DESC(ca, it);
.LBB0_25:
	s_mul_i32 s6, s58, 15
	s_add_i32 s2, s6, 1
	s_cmp_gt_i32 s77, s2
	s_cselect_b64 s[0:1], -1, 0
	s_add_i32 s3, s6, 16
	s_cmp_lt_i32 s76, s3
	s_cselect_b64 s[4:5], -1, 0
	s_and_b64 s[0:1], s[0:1], s[4:5]
	s_andn2_b64 vcc, exec, s[0:1]
	s_cbranch_vccnz .LBB0_24
	v_writelane_b32 v254, s6, 36
	v_writelane_b32 v254, s3, 37
	s_mov_b32 s3, s2
	s_cmp_gt_i32 s76, s3
	s_cselect_b64 s[0:1], -1, 0
	s_cmp_ge_i32 s3, s77
	s_cselect_b64 s[4:5], -1, 0
	s_or_b64 s[0:1], s[0:1], s[4:5]
	v_writelane_b32 v254, s58, 38
	s_and_b64 vcc, exec, s[0:1]
	s_cbranch_vccnz .LBB0_92
	s_cmp_gt_u32 s58, 0
	s_cbranch_scc1 .LBB0_92
	s_movk_i32 s99, 0x1580
	v_readlane_b32 s0, v254, 8
	v_readlane_b32 s4, v254, 10
	v_readlane_b32 s1, v254, 9
	v_mbcnt_lo_u32_b32 v11, -1, 0
	v_mbcnt_hi_u32_b32 v11, -1, v11
	s_load_dword s6, s[0:1], 0x0
	s_mov_b32 s3, s84
	s_waitcnt lgkmcnt(0)
	s_lshl_b32 s3, s3, 3
	v_readlane_b32 s0, v254, 0
	s_add_i32 s3, s3, s4
	v_readlane_b32 s1, v254, 1
	s_cmp_ge_i32 s3, s99
	s_cbranch_scc1 .Lmy_p0_second
	s_load_dwordx2 s[8:9], s[0:1], 0x138
	v_readlane_b32 s14, v254, 38
	s_mulk_i32 s4, 0x4100
	s_add_i32 s7, s4, 0
	v_sub_u32_e64 v0, s14, 1 clamp
	s_lshl_b32 s33, s6, 3
	v_readfirstlane_b32 s4, v0
	s_lshl_b32 s96, s4, 16
	s_waitcnt lgkmcnt(0)
	s_add_u32 s4, s8, 0x22800000
	s_addc_u32 s5, s9, 0
	v_writelane_b32 v254, s4, 39
	s_mov_b32 s15, s97
	v_and_b32_e32 v0, 7, v11
	v_writelane_b32 v254, s5, 40
	s_add_u32 s4, s8, 0x22780000
	s_addc_u32 s5, s9, 0
	v_writelane_b32 v254, s4, 41
	v_ashrrev_i32_e32 v13, 3, v11
	v_lshlrev_b32_e32 v10, 3, v0
	v_writelane_b32 v254, s5, 42
	s_lshl_b32 s4, s14, 18
	s_add_u32 s10, s8, 0x22700000
	s_addc_u32 s11, s9, 0
	v_writelane_b32 v254, s10, 43
	s_mov_b32 s5, s97
	v_mul_u32_u24_e32 v0, 0x820, v0
	v_writelane_b32 v254, s11, 44
	s_mul_i32 s10, s14, 0x18000
	s_mov_b32 s11, s97
	v_writelane_b32 v254, s10, 45
	v_lshlrev_b32_e32 v1, 2, v13
	v_lshl_add_u32 v12, v11, 2, s7
	v_writelane_b32 v254, s11, 46
	s_add_u32 s10, s8, 0x22680000
	s_addc_u32 s11, s9, 0
	v_writelane_b32 v254, s10, 47
	v_add3_u32 v14, s7, v0, v1
	s_mov_b32 s41, s97
	v_writelane_b32 v254, s11, 48
	s_add_u32 s10, s8, 0x22600000
	s_addc_u32 s11, s9, 0
	v_writelane_b32 v254, s10, 49
	s_nop 1
	v_writelane_b32 v254, s11, 50
	s_lshl_b32 s10, s14, 20
	s_mov_b32 s11, s97
	v_writelane_b32 v254, s10, 51
	s_nop 1
	v_writelane_b32 v254, s11, 52
	s_add_u32 s10, s8, 0x22400000
	s_addc_u32 s11, s9, 0
	v_writelane_b32 v254, s10, 53
	s_nop 1
	v_writelane_b32 v254, s11, 54
	s_lshl_b32 s10, s14, 21
	s_mov_b32 s11, s97
	v_writelane_b32 v254, s10, 55
	s_nop 1
	v_writelane_b32 v254, s11, 56
	s_add_u32 s10, s8, 0x22e80000
	s_addc_u32 s11, s9, 0
	v_writelane_b32 v254, s10, 57
	s_nop 1
	v_writelane_b32 v254, s11, 58
	s_add_u32 s10, s8, 0x27b80000
	s_addc_u32 s11, s9, 0
	v_writelane_b32 v254, s10, 59
	s_nop 1
	v_writelane_b32 v254, s11, 60
	s_add_u32 s10, s8, 0x22880000
	s_addc_u32 s11, s9, 0
	v_writelane_b32 v254, s10, 61
	s_nop 1
	v_writelane_b32 v254, s11, 62
	s_lshl_b32 s10, s14, 22
	s_add_u32 s12, s8, 0x23280000
	s_addc_u32 s13, s9, 0
	v_writelane_b32 v254, s12, 63
	s_mov_b32 s11, s97
	s_nop 0
	v_writelane_b32 v255, s13, 0
	s_mul_i32 s12, s14, 0xac0000
	s_mov_b32 s13, s97
	v_writelane_b32 v255, s12, 1
	s_nop 1
	v_writelane_b32 v255, s13, 2
	s_add_u32 s12, s8, 0x26580000
	s_addc_u32 s13, s9, 0
	v_writelane_b32 v255, s12, 3
	s_nop 1
	v_writelane_b32 v255, s13, 4
	s_add_u32 s12, s8, 0x1d200000
	s_addc_u32 s13, s9, 0
	s_lshl_b32 s40, s14, 11
	v_writelane_b32 v255, s12, 5
	s_add_u32 s16, s8, 0x1e800000
	s_addc_u32 s17, s9, 0
	v_writelane_b32 v255, s13, 6
	v_writelane_b32 v255, s16, 7
	s_mul_i32 s12, s14, 0x1de0000
	s_mul_i32 s14, s14, 0x1580000
	v_writelane_b32 v255, s17, 8
	v_writelane_b32 v255, s14, 9
	s_mov_b32 s13, s97
	s_nop 0
	v_writelane_b32 v255, s15, 10
	s_add_u32 s14, s8, 0x23a80000
	s_addc_u32 s15, s9, 0
	v_writelane_b32 v255, s14, 11
	s_add_u32 s8, s8, 0x1a700000
	s_addc_u32 s9, s9, 0
	v_writelane_b32 v255, s15, 12
	v_writelane_b32 v255, s8, 13
	s_lshl_b64 s[4:5], s[4:5], 2
	s_lshl_b32 s7, s3, 4
	v_writelane_b32 v255, s9, 14
	v_writelane_b32 v255, s4, 15
	s_add_i32 s72, s7, 0xc00
	s_lshl_b32 s7, s3, 1
	v_writelane_b32 v255, s5, 16
	s_lshl_b64 s[4:5], s[10:11], 2
	v_writelane_b32 v255, s4, 17
	s_lshl_b32 s66, s3, 6
	s_lshl_b32 s67, s6, 9
	v_writelane_b32 v255, s5, 18
	s_lshl_b64 s[4:5], s[12:13], 2
	v_writelane_b32 v255, s4, 19
	s_lshl_b32 s68, s3, 5
	s_lshl_b32 s69, s6, 8
	v_writelane_b32 v255, s5, 20
	v_writelane_b32 v255, s80, 21
	s_lshl_b32 s70, s3, 2
	s_lshl_b32 s71, s6, 5
	v_writelane_b32 v255, s81, 22
	v_writelane_b32 v255, s82, 23
	s_lshl_b32 s73, s6, 7
	s_add_i32 s74, s7, 0x13500
	s_lshl_b32 s75, s6, 4
	v_writelane_b32 v255, s83, 24
	s_branch .LBB0_31

; __device__ __forceinline__ unsigned xb_add(unsigned* p, unsigned v) { return __hip_atomic_fetch_add(p, v, __ATOMIC_RELAXED, __HIP_MEMORY_SCOPE_AGENT); }
; __device__ __forceinline__ void xcd_barrier(const XcdBarrier& b) {
;     asm volatile("s_waitcnt vmcnt(0)" ::: "memory");
;     __syncthreads();
;     if (threadIdx.x == 0) {
;         unsigned* bar = b.bar;
;         __builtin_amdgcn_s_waitcnt(0);
;         unsigned nloc = b.st[0], nx = b.st[1];
;         if (nloc == 0u) { xcd_barrier_complete(bar, b.x, nloc, nx); b.st[0] = nloc; b.st[1] = nx; }
;         const unsigned old = xb_add(&bar[XB_XSUB(b.x)], 1u);
.Lcvp0c_ret:
.LBB0_92:
	s_cmp_gt_i32 s76, s2
	s_cselect_b64 s[0:1], -1, 0
	s_cmp_ge_i32 s2, s77
	s_cselect_b64 s[2:3], -1, 0
	v_readlane_b32 s53, v254, 36
	s_or_b64 s[0:1], s[0:1], s[2:3]
	s_add_i32 s38, s53, 2
	s_and_b64 vcc, exec, s[0:1]
	s_movk_i32 s70, 0xad
	v_readlane_b32 s98, v254, 38
	s_nop 3
	s_cmp_gt_u32 s98, 0
	s_cbranch_scc1 .LBB0_125
	s_cbranch_vccnz .LBB0_125
	s_mov_b32 s2, s38
	s_cmp_le_i32 s76, s2
	s_cselect_b64 s[0:1], -1, 0
	s_cmp_lt_i32 s2, s77
	s_cselect_b64 s[2:3], -1, 0
	s_and_b64 s[0:1], s[0:1], s[2:3]
	v_readlane_b32 s2, v254, 4
	v_readlane_b32 s3, v254, 5
	s_and_b64 s[0:1], s[2:3], s[0:1]
	s_andn2_b64 vcc, exec, s[0:1]
	s_cbranch_vccnz .LBB0_125
	v_readlane_b32 s36, v254, 2
	v_readlane_b32 s37, v254, 3
	v_readlane_b32 s33, v254, 6
	s_waitcnt vmcnt(0)
	s_waitcnt lgkmcnt(0)
	s_barrier
	s_mov_b64 s[0:1], exec
	v_readlane_b32 s2, v254, 13
	v_readlane_b32 s3, v254, 14
	s_and_b64 s[2:3], s[0:1], s[2:3]
	s_mov_b64 exec, s[2:3]
	s_cbranch_execz .LBB0_124
	v_readlane_b32 s2, v254, 7
	s_waitcnt vmcnt(0) expcnt(0) lgkmcnt(0)
	s_nop 0
	v_mov_b32_e32 v0, s2
	ds_read_b32 v2, v0
	ds_read_b32 v0, v0 offset:4
	s_waitcnt lgkmcnt(1)
	v_cmp_ne_u32_e32 vcc, 0, v2
	s_cbranch_vccnz .LBB0_109
	v_readlane_b32 s4, v254, 8
	v_readlane_b32 s5, v254, 9
	s_load_dwordx2 s[2:3], s[4:5], 0x0
	s_load_dword s7, s[4:5], 0x8
	s_add_u32 s4, s36, 0x1000
	s_addc_u32 s5, s37, 0
	s_add_u32 s6, s36, 0x1100
	s_waitcnt lgkmcnt(0)
	s_mul_i32 s30, s3, s2
	s_mul_i32 s30, s30, s7
	s_addc_u32 s7, s37, 0
	s_add_u32 s8, s36, 0x1200
	s_addc_u32 s9, s37, 0
	s_add_u32 s10, s36, 0x1300
	s_addc_u32 s11, s37, 0
	s_mov_b32 s31, 1
	s_mov_b64 s[12:13], 0
	s_branch .LBB0_99

; #define LAS __attribute__((address_space(3)))
; __global__ void __launch_bounds__(NWAVES * 64, 2) mk_fwd(Args args) {
;     ...
;             PH_LOCALS
;             LAS float* scr = (LAS float*)(lds + RING_OFF + wave * 16640);   static_assert(8 * 16640 <= LDSCTL_OFF, "converter scratch below the LDS control words");
;             constexpr int I_UP = (D / 64) * (NUP / 64), I_DN = (DFF / 64) * (D / 64), I_IN = (D / 64) * (DINP / 64), I_GLU = 16 * 16, I_L = 4 * 16, I_V1 = 16 * 4, I_V2 = 4 * 16,
;                           I_BS5 = 16 * 32, I_BAT = 8 * 32, I_BRW = 16 * 32, I_OUT = 32 * 32;
;             constexpr int NITEMS = 2 * I_UP + 2 * I_DN + I_IN + I_GLU + 3 * I_L + I_V1 + I_V2 + I_BS5 + I_BAT + I_BRW + I_OUT;
;             const int lv = l > 0 ? l - 1 : 0;
;     ...
;             for (int it = gw; it < NITEMS; it += NGW) {
;                 ConvItem ca; CONV_DESC(ca, it);
.Lcvp10_ret:
.Lcvrs_p10:
	v_readlane_b32 s0, v254, 8
	v_readlane_b32 s4, v254, 10
	v_readlane_b32 s1, v254, 9
	v_mbcnt_lo_u32_b32 v11, -1, 0
	v_mbcnt_hi_u32_b32 v11, -1, v11
	s_load_dword s6, s[0:1], 0x0
	s_mov_b32 s3, s84
	s_waitcnt lgkmcnt(0)
	s_movk_i32 s6, 160
	s_lshl_b32 s3, s3, 3
	v_readlane_b32 s0, v254, 0
	s_add_i32 s3, s3, s4
	s_add_i32 s3, s3, 0x5b80
	v_readlane_b32 s1, v254, 1
	s_cmpk_gt_i32 s3, 26495
	s_cbranch_scc1 .Lcvp11_ret
	s_load_dwordx2 s[8:9], s[0:1], 0x138
	v_readlane_b32 s14, v254, 38
	s_mulk_i32 s4, 0x4100
	s_add_i32 s7, s4, 0
	v_sub_u32_e64 v0, s14, 1 clamp
	s_lshl_b32 s33, s6, 3
	v_readfirstlane_b32 s4, v0
	s_lshl_b32 s96, s4, 16
	s_waitcnt lgkmcnt(0)
	s_add_u32 s4, s8, 0x22800000
	s_addc_u32 s5, s9, 0
	v_writelane_b32 v254, s4, 39
	s_mov_b32 s15, s97
	v_and_b32_e32 v0, 7, v11
	v_writelane_b32 v254, s5, 40
	s_add_u32 s4, s8, 0x22780000
	s_addc_u32 s5, s9, 0
	v_writelane_b32 v254, s4, 41
	v_ashrrev_i32_e32 v13, 3, v11
	v_lshlrev_b32_e32 v10, 3, v0
	v_writelane_b32 v254, s5, 42
	s_lshl_b32 s4, s14, 18
	s_add_u32 s10, s8, 0x22700000
	s_addc_u32 s11, s9, 0
	v_writelane_b32 v254, s10, 43
	s_mov_b32 s5, s97
	v_mul_u32_u24_e32 v0, 0x820, v0
	v_writelane_b32 v254, s11, 44
	s_mul_i32 s10, s14, 0x18000
	s_mov_b32 s11, s97
	v_writelane_b32 v254, s10, 45
	v_lshlrev_b32_e32 v1, 2, v13
	v_lshl_add_u32 v12, v11, 2, s7
	v_writelane_b32 v254, s11, 46
	s_add_u32 s10, s8, 0x22680000
	s_addc_u32 s11, s9, 0
	v_writelane_b32 v254, s10, 47
	v_add3_u32 v14, s7, v0, v1
	s_mov_b32 s41, s97
	v_writelane_b32 v254, s11, 48
	s_add_u32 s10, s8, 0x22600000
	s_addc_u32 s11, s9, 0
	v_writelane_b32 v254, s10, 49
	s_nop 1
	v_writelane_b32 v254, s11, 50
	s_lshl_b32 s10, s14, 20
	s_mov_b32 s11, s97
	v_writelane_b32 v254, s10, 51
	s_nop 1
	v_writelane_b32 v254, s11, 52
	s_add_u32 s10, s8, 0x22400000
	s_addc_u32 s11, s9, 0
	v_writelane_b32 v254, s10, 53
	s_nop 1
	v_writelane_b32 v254, s11, 54
	s_lshl_b32 s10, s14, 21
	s_mov_b32 s11, s97
	v_writelane_b32 v254, s10, 55
	s_nop 1
	v_writelane_b32 v254, s11, 56
	s_add_u32 s10, s8, 0x22e80000
	s_addc_u32 s11, s9, 0
	v_writelane_b32 v254, s10, 57
	s_nop 1
	v_writelane_b32 v254, s11, 58
	s_add_u32 s10, s8, 0x27b80000
	s_addc_u32 s11, s9, 0
	v_writelane_b32 v254, s10, 59
	s_nop 1
	v_writelane_b32 v254, s11, 60
	s_add_u32 s10, s8, 0x22880000
	s_addc_u32 s11, s9, 0
	v_writelane_b32 v254, s10, 61
	s_nop 1
	v_writelane_b32 v254, s11, 62
	s_lshl_b32 s10, s14, 22
	s_add_u32 s12, s8, 0x23280000
	s_addc_u32 s13, s9, 0
	v_writelane_b32 v254, s12, 63
	s_mov_b32 s11, s97
	s_nop 0
	v_writelane_b32 v255, s13, 0
	s_mul_i32 s12, s14, 0xac0000
	s_mov_b32 s13, s97
	v_writelane_b32 v255, s12, 1
	s_nop 1
	v_writelane_b32 v255, s13, 2
	s_add_u32 s12, s8, 0x26580000
	s_addc_u32 s13, s9, 0
	v_writelane_b32 v255, s12, 3
	s_nop 1
	v_writelane_b32 v255, s13, 4
	s_add_u32 s12, s8, 0x1d200000
	s_addc_u32 s13, s9, 0
	s_lshl_b32 s40, s14, 11
	v_writelane_b32 v255, s12, 5
	s_add_u32 s16, s8, 0x1e800000
	s_addc_u32 s17, s9, 0
	v_writelane_b32 v255, s13, 6
	v_writelane_b32 v255, s16, 7
	s_mul_i32 s12, s14, 0x1de0000
	s_mul_i32 s14, s14, 0x1580000
	v_writelane_b32 v255, s17, 8
	v_writelane_b32 v255, s14, 9
	s_mov_b32 s13, s97
	s_nop 0
	v_writelane_b32 v255, s15, 10
	s_add_u32 s14, s8, 0x23a80000
	s_addc_u32 s15, s9, 0
	v_writelane_b32 v255, s14, 11
	s_add_u32 s8, s8, 0x1a700000
	s_addc_u32 s9, s9, 0
	v_writelane_b32 v255, s15, 12
	v_writelane_b32 v255, s8, 13
	s_lshl_b64 s[4:5], s[4:5], 2
	s_lshl_b32 s7, s3, 4
	v_writelane_b32 v255, s9, 14
	v_writelane_b32 v255, s4, 15
	s_add_i32 s72, s7, 0xc00
	s_lshl_b32 s7, s3, 1
	v_writelane_b32 v255, s5, 16
	s_lshl_b64 s[4:5], s[10:11], 2
	v_writelane_b32 v255, s4, 17
	s_lshl_b32 s66, s3, 6
	s_lshl_b32 s67, s6, 9
	v_writelane_b32 v255, s5, 18
	s_lshl_b64 s[4:5], s[12:13], 2
	v_writelane_b32 v255, s4, 19
	s_lshl_b32 s68, s3, 5
	s_lshl_b32 s69, s6, 8
	v_writelane_b32 v255, s5, 20
	v_writelane_b32 v255, s80, 21
	s_lshl_b32 s70, s3, 2
	s_lshl_b32 s71, s6, 5
	v_writelane_b32 v255, s81, 22
	v_writelane_b32 v255, s82, 23
	s_lshl_b32 s73, s6, 7
	s_add_i32 s74, s7, 0x13500
	s_lshl_b32 s75, s6, 4
	v_writelane_b32 v255, s83, 24
	s_branch .Lcvp11_31

; #define LAS __attribute__((address_space(3)))
; __global__ void __launch_bounds__(NWAVES * 64, 2) mk_fwd(Args args) {
;     ...
;             PH_LOCALS
;             LAS float* scr = (LAS float*)(lds + RING_OFF + wave * 16640);   static_assert(8 * 16640 <= LDSCTL_OFF, "converter scratch below the LDS control words");
;             constexpr int I_UP = (D / 64) * (NUP / 64), I_DN = (DFF / 64) * (D / 64), I_IN = (D / 64) * (DINP / 64), I_GLU = 16 * 16, I_L = 4 * 16, I_V1 = 16 * 4, I_V2 = 4 * 16,
;                           I_BS5 = 16 * 32, I_BAT = 8 * 32, I_BRW = 16 * 32, I_OUT = 32 * 32;
;             constexpr int NITEMS = 2 * I_UP + 2 * I_DN + I_IN + I_GLU + 3 * I_L + I_V1 + I_V2 + I_BS5 + I_BAT + I_BRW + I_OUT;
;             const int lv = l > 0 ? l - 1 : 0;
;     ...
;             for (int it = gw; it < NITEMS; it += NGW) {
;                 ConvItem ca; CONV_DESC(ca, it);
.Lcvp30_ret:
.Lcvrs_p30:
	v_readlane_b32 s0, v254, 8
	v_readlane_b32 s4, v254, 10
	v_readlane_b32 s1, v254, 9
	v_mbcnt_lo_u32_b32 v11, -1, 0
	v_mbcnt_hi_u32_b32 v11, -1, v11
	s_load_dword s6, s[0:1], 0x0
	s_mov_b32 s3, s84
	s_waitcnt lgkmcnt(0)
	s_movk_i32 s6, 128
	s_lshl_b32 s3, s3, 3
	v_readlane_b32 s0, v254, 0
	s_add_i32 s3, s3, s4
	s_add_i32 s3, s3, 0x4fc0
	v_readlane_b32 s1, v254, 1
	s_cmpk_gt_i32 s3, 24191
	s_cbranch_scc1 .Lcvp31_ret
	s_load_dwordx2 s[8:9], s[0:1], 0x138
	v_readlane_b32 s14, v254, 38
	s_mulk_i32 s4, 0x4100
	s_add_i32 s7, s4, 0
	v_sub_u32_e64 v0, s14, 1 clamp
	s_lshl_b32 s33, s6, 3
	v_readfirstlane_b32 s4, v0
	s_lshl_b32 s96, s4, 16
	s_waitcnt lgkmcnt(0)
	s_add_u32 s4, s8, 0x22800000
	s_addc_u32 s5, s9, 0
	v_writelane_b32 v254, s4, 39
	s_mov_b32 s15, s97
	v_and_b32_e32 v0, 7, v11
	v_writelane_b32 v254, s5, 40
	s_add_u32 s4, s8, 0x22780000
	s_addc_u32 s5, s9, 0
	v_writelane_b32 v254, s4, 41
	v_ashrrev_i32_e32 v13, 3, v11
	v_lshlrev_b32_e32 v10, 3, v0
	v_writelane_b32 v254, s5, 42
	s_lshl_b32 s4, s14, 18
	s_add_u32 s10, s8, 0x22700000
	s_addc_u32 s11, s9, 0
	v_writelane_b32 v254, s10, 43
	s_mov_b32 s5, s97
	v_mul_u32_u24_e32 v0, 0x820, v0
	v_writelane_b32 v254, s11, 44
	s_mul_i32 s10, s14, 0x18000
	s_mov_b32 s11, s97
	v_writelane_b32 v254, s10, 45
	v_lshlrev_b32_e32 v1, 2, v13
	v_lshl_add_u32 v12, v11, 2, s7
	v_writelane_b32 v254, s11, 46
	s_add_u32 s10, s8, 0x22680000
	s_addc_u32 s11, s9, 0
	v_writelane_b32 v254, s10, 47
	v_add3_u32 v14, s7, v0, v1
	s_mov_b32 s41, s97
	v_writelane_b32 v254, s11, 48
	s_add_u32 s10, s8, 0x22600000
	s_addc_u32 s11, s9, 0
	v_writelane_b32 v254, s10, 49
	s_nop 1
	v_writelane_b32 v254, s11, 50
	s_lshl_b32 s10, s14, 20
	s_mov_b32 s11, s97
	v_writelane_b32 v254, s10, 51
	s_nop 1
	v_writelane_b32 v254, s11, 52
	s_add_u32 s10, s8, 0x22400000
	s_addc_u32 s11, s9, 0
	v_writelane_b32 v254, s10, 53
	s_nop 1
	v_writelane_b32 v254, s11, 54
	s_lshl_b32 s10, s14, 21
	s_mov_b32 s11, s97
	v_writelane_b32 v254, s10, 55
	s_nop 1
	v_writelane_b32 v254, s11, 56
	s_add_u32 s10, s8, 0x22e80000
	s_addc_u32 s11, s9, 0
	v_writelane_b32 v254, s10, 57
	s_nop 1
	v_writelane_b32 v254, s11, 58
	s_add_u32 s10, s8, 0x27b80000
	s_addc_u32 s11, s9, 0
	v_writelane_b32 v254, s10, 59
	s_nop 1
	v_writelane_b32 v254, s11, 60
	s_add_u32 s10, s8, 0x22880000
	s_addc_u32 s11, s9, 0
	v_writelane_b32 v254, s10, 61
	s_nop 1
	v_writelane_b32 v254, s11, 62
	s_lshl_b32 s10, s14, 22
	s_add_u32 s12, s8, 0x23280000
	s_addc_u32 s13, s9, 0
	v_writelane_b32 v254, s12, 63
	s_mov_b32 s11, s97
	s_nop 0
	v_writelane_b32 v255, s13, 0
	s_mul_i32 s12, s14, 0xac0000
	s_mov_b32 s13, s97
	v_writelane_b32 v255, s12, 1
	s_nop 1
	v_writelane_b32 v255, s13, 2
	s_add_u32 s12, s8, 0x26580000
	s_addc_u32 s13, s9, 0
	v_writelane_b32 v255, s12, 3
	s_nop 1
	v_writelane_b32 v255, s13, 4
	s_add_u32 s12, s8, 0x1d200000
	s_addc_u32 s13, s9, 0
	s_lshl_b32 s40, s14, 11
	v_writelane_b32 v255, s12, 5
	s_add_u32 s16, s8, 0x1e800000
	s_addc_u32 s17, s9, 0
	v_writelane_b32 v255, s13, 6
	v_writelane_b32 v255, s16, 7
	s_mul_i32 s12, s14, 0x1de0000
	s_mul_i32 s14, s14, 0x1580000
	v_writelane_b32 v255, s17, 8
	v_writelane_b32 v255, s14, 9
	s_mov_b32 s13, s97
	s_nop 0
	v_writelane_b32 v255, s15, 10
	s_add_u32 s14, s8, 0x23a80000
	s_addc_u32 s15, s9, 0
	v_writelane_b32 v255, s14, 11
	s_add_u32 s8, s8, 0x1a700000
	s_addc_u32 s9, s9, 0
	v_writelane_b32 v255, s15, 12
	v_writelane_b32 v255, s8, 13
	s_lshl_b64 s[4:5], s[4:5], 2
	s_lshl_b32 s7, s3, 4
	v_writelane_b32 v255, s9, 14
	v_writelane_b32 v255, s4, 15
	s_add_i32 s72, s7, 0xc00
	s_lshl_b32 s7, s3, 1
	v_writelane_b32 v255, s5, 16
	s_lshl_b64 s[4:5], s[10:11], 2
	v_writelane_b32 v255, s4, 17
	s_lshl_b32 s66, s3, 6
	s_lshl_b32 s67, s6, 9
	v_writelane_b32 v255, s5, 18
	s_lshl_b64 s[4:5], s[12:13], 2
	v_writelane_b32 v255, s4, 19
	s_lshl_b32 s68, s3, 5
	s_lshl_b32 s69, s6, 8
	v_writelane_b32 v255, s5, 20
	v_writelane_b32 v255, s80, 21
	s_lshl_b32 s70, s3, 2
	s_lshl_b32 s71, s6, 5
	v_writelane_b32 v255, s81, 22
	v_writelane_b32 v255, s82, 23
	s_lshl_b32 s73, s6, 7
	s_add_i32 s74, s7, 0x13500
	s_lshl_b32 s75, s6, 4
	v_writelane_b32 v255, s83, 24
	s_branch .Lcvp31_31

; #define LAS __attribute__((address_space(3)))
; __device__ __forceinline__ void conv_load(const ConvItem& ci, int lane, float (&v)[64]) {
;     ...
;     for (int i = 0; i < 64; ++i) { const int k = ci.k0 + i, kk = k < kmax ? k : kmax; v[i] = __builtin_nontemporal_load(base + (size_t)kk * ci.ldw); }
; #pragma unroll
;     for (int i = 0; i < 64; ++i) v[i] = (okc && (ci.k0 + i) < ci.Ksrc) ? v[i] : 0.f;
; }
; __device__ __forceinline__ void conv_store(const ConvItem& ci, LAS float* scr, int lane, const float (&v)[64]) {
;     const int c = lane & 7;
;     f32x4 s0 = {1.f, 1.f, 1.f, 1.f}, s1 = s0;
;     if (ci.ks) { const int kb = ci.k0 + 8 * c < ci.Ksrc - 8 ? ci.k0 + 8 * c : ci.Ksrc - 8; s0 = *(const f32x4*)(ci.ks + kb); s1 = *(const f32x4*)(ci.ks + kb + 4); }
; #pragma unroll
;     for (int i = 0; i < 64; ++i) scr[i * 65 + lane] = v[i];
.Lcvp31_30:
	s_cmp_lt_i32 s58, s76
	s_cselect_b64 s[4:5], -1, 0
	s_and_b64 s[4:5], vcc, s[4:5]
	s_cmp_lt_i32 s64, s76
	s_waitcnt vmcnt(62)
	v_cndmask_b32_e64 v21, 0, v21, s[4:5]
	s_cselect_b64 s[4:5], -1, 0
	s_and_b64 s[4:5], vcc, s[4:5]
	s_cmp_lt_i32 s65, s76
	v_cndmask_b32_e64 v20, 0, v20, s[4:5]
	s_cselect_b64 s[4:5], -1, 0
	s_and_b64 s[4:5], vcc, s[4:5]
	s_cmp_lt_i32 s78, s76
	s_waitcnt vmcnt(61)
	v_cndmask_b32_e64 v19, 0, v19, s[4:5]
	s_cselect_b64 s[4:5], -1, 0
	s_and_b64 s[4:5], vcc, s[4:5]
	s_cmp_lt_i32 s79, s76
	s_waitcnt vmcnt(60)
	v_cndmask_b32_e64 v18, 0, v18, s[4:5]
	s_cselect_b64 s[4:5], -1, 0
	s_and_b64 s[4:5], vcc, s[4:5]
	s_cmp_lt_i32 s80, s76
	s_waitcnt vmcnt(59)
	v_cndmask_b32_e64 v17, 0, v17, s[4:5]
	s_cselect_b64 s[4:5], -1, 0
	s_and_b64 s[4:5], vcc, s[4:5]
	s_cmp_lt_i32 s81, s76
	s_waitcnt vmcnt(58)
	v_cndmask_b32_e64 v16, 0, v16, s[4:5]
	s_cselect_b64 s[4:5], -1, 0
	s_and_b64 s[4:5], vcc, s[4:5]
	s_cmp_lt_i32 s82, s76
	s_waitcnt vmcnt(57)
	v_cndmask_b32_e64 v15, 0, v15, s[4:5]
	s_cselect_b64 s[4:5], -1, 0
	s_and_b64 s[4:5], vcc, s[4:5]
	s_cmp_lt_i32 s83, s76
	s_waitcnt vmcnt(56)
	v_cndmask_b32_e64 v8, 0, v8, s[4:5]
	s_cselect_b64 s[4:5], -1, 0
	s_and_b64 s[4:5], vcc, s[4:5]
	s_cmp_lt_i32 s85, s76
	s_waitcnt vmcnt(55)
	v_cndmask_b32_e64 v29, 0, v29, s[4:5]
	s_cselect_b64 s[4:5], -1, 0
	s_and_b64 s[4:5], vcc, s[4:5]
	s_cmp_lt_i32 s86, s76
	s_waitcnt vmcnt(54)
	v_cndmask_b32_e64 v28, 0, v28, s[4:5]
	s_cselect_b64 s[4:5], -1, 0
	s_and_b64 s[4:5], vcc, s[4:5]
	s_cmp_lt_i32 s87, s76
	s_waitcnt vmcnt(53)
	v_cndmask_b32_e64 v27, 0, v27, s[4:5]
	s_cselect_b64 s[4:5], -1, 0
	s_and_b64 s[4:5], vcc, s[4:5]
	s_cmp_lt_i32 s88, s76
	s_waitcnt vmcnt(52)
	v_cndmask_b32_e64 v26, 0, v26, s[4:5]
	s_cselect_b64 s[4:5], -1, 0
	s_and_b64 s[4:5], vcc, s[4:5]
	s_cmp_lt_i32 s89, s76
	s_waitcnt vmcnt(51)
	v_cndmask_b32_e64 v25, 0, v25, s[4:5]
	s_cselect_b64 s[4:5], -1, 0
	s_and_b64 s[4:5], vcc, s[4:5]
	s_cmp_lt_i32 s90, s76
	s_waitcnt vmcnt(50)
	v_cndmask_b32_e64 v24, 0, v24, s[4:5]
	s_cselect_b64 s[4:5], -1, 0
	s_and_b64 s[4:5], vcc, s[4:5]
	s_cmp_lt_i32 s92, s76
	s_waitcnt vmcnt(49)
	v_cndmask_b32_e64 v23, 0, v23, s[4:5]
	s_cselect_b64 s[4:5], -1, 0
	s_and_b64 s[4:5], vcc, s[4:5]
	s_cmp_lt_i32 s93, s76
	s_waitcnt vmcnt(48)
	v_cndmask_b32_e64 v22, 0, v22, s[4:5]
	s_cselect_b64 s[4:5], -1, 0
	s_and_b64 s[4:5], vcc, s[4:5]
	s_cmp_lt_i32 s94, s76
	s_waitcnt vmcnt(47)
	v_cndmask_b32_e64 v37, 0, v37, s[4:5]
	s_cselect_b64 s[4:5], -1, 0
	s_and_b64 s[4:5], vcc, s[4:5]
	s_cmp_lt_i32 s95, s76
	s_waitcnt vmcnt(46)
	v_cndmask_b32_e64 v36, 0, v36, s[4:5]
	s_cselect_b64 s[4:5], -1, 0
	s_and_b64 s[4:5], vcc, s[4:5]
	s_cmp_lt_i32 s50, s76
	s_waitcnt vmcnt(45)
	v_cndmask_b32_e64 v35, 0, v35, s[4:5]
	s_cselect_b64 s[4:5], -1, 0
	s_and_b64 s[4:5], vcc, s[4:5]
	s_cmp_lt_i32 s51, s76
	s_waitcnt vmcnt(44)
	v_cndmask_b32_e64 v34, 0, v34, s[4:5]
	s_cselect_b64 s[4:5], -1, 0
	s_and_b64 s[4:5], vcc, s[4:5]
	s_cmp_lt_i32 s52, s76
	s_waitcnt vmcnt(43)
	v_cndmask_b32_e64 v33, 0, v33, s[4:5]
	s_cselect_b64 s[4:5], -1, 0
	s_and_b64 s[4:5], vcc, s[4:5]
	s_cmp_lt_i32 s53, s76
	s_waitcnt vmcnt(42)
	v_cndmask_b32_e64 v32, 0, v32, s[4:5]
	s_cselect_b64 s[4:5], -1, 0
	s_and_b64 s[4:5], vcc, s[4:5]
	s_cmp_lt_i32 s6, s76
	s_waitcnt vmcnt(41)
	v_cndmask_b32_e64 v31, 0, v31, s[4:5]
	s_cselect_b64 s[4:5], -1, 0
	s_and_b64 s[4:5], vcc, s[4:5]
	s_cmp_lt_i32 s7, s76
	s_waitcnt vmcnt(40)
	v_cndmask_b32_e64 v30, 0, v30, s[4:5]
	s_cselect_b64 s[4:5], -1, 0
	s_and_b64 s[4:5], vcc, s[4:5]
	s_cmp_lt_i32 s8, s76
	s_waitcnt vmcnt(39)
	v_cndmask_b32_e64 v45, 0, v45, s[4:5]
	s_cselect_b64 s[4:5], -1, 0
	s_and_b64 s[4:5], vcc, s[4:5]
	s_cmp_lt_i32 s9, s76
	s_waitcnt vmcnt(38)
	v_cndmask_b32_e64 v44, 0, v44, s[4:5]
	s_cselect_b64 s[4:5], -1, 0
	s_and_b64 s[4:5], vcc, s[4:5]
	s_cmp_lt_i32 s10, s76
	s_waitcnt vmcnt(37)
	v_cndmask_b32_e64 v43, 0, v43, s[4:5]
	s_cselect_b64 s[4:5], -1, 0
	s_and_b64 s[4:5], vcc, s[4:5]
	s_cmp_lt_i32 s11, s76
	s_waitcnt vmcnt(36)
	v_cndmask_b32_e64 v42, 0, v42, s[4:5]
	s_cselect_b64 s[4:5], -1, 0
	s_and_b64 s[4:5], vcc, s[4:5]
	s_cmp_lt_i32 s14, s76
	s_waitcnt vmcnt(35)
	v_cndmask_b32_e64 v41, 0, v41, s[4:5]
	s_cselect_b64 s[4:5], -1, 0
	s_and_b64 s[4:5], vcc, s[4:5]
	s_cmp_lt_i32 s15, s76
	s_waitcnt vmcnt(34)
	v_cndmask_b32_e64 v40, 0, v40, s[4:5]
	s_cselect_b64 s[4:5], -1, 0
	s_and_b64 s[4:5], vcc, s[4:5]
	s_cmp_lt_i32 s16, s76
	s_waitcnt vmcnt(33)
	v_cndmask_b32_e64 v39, 0, v39, s[4:5]
	s_cselect_b64 s[4:5], -1, 0
	s_and_b64 s[4:5], vcc, s[4:5]
	s_cmp_lt_i32 s17, s76
	s_waitcnt vmcnt(32)
	v_cndmask_b32_e64 v38, 0, v38, s[4:5]
	s_cselect_b64 s[4:5], -1, 0
	s_and_b64 s[4:5], vcc, s[4:5]
	s_cmp_lt_i32 s12, s76
	s_waitcnt vmcnt(31)
	v_cndmask_b32_e64 v53, 0, v53, s[4:5]
	s_cselect_b64 s[4:5], -1, 0
	s_and_b64 s[4:5], vcc, s[4:5]
	s_cmp_lt_i32 s13, s76
	s_waitcnt vmcnt(30)
	v_cndmask_b32_e64 v52, 0, v52, s[4:5]
	s_cselect_b64 s[4:5], -1, 0
	s_and_b64 s[4:5], vcc, s[4:5]
	s_cmp_lt_i32 s20, s76
	s_waitcnt vmcnt(29)
	v_cndmask_b32_e64 v51, 0, v51, s[4:5]
	s_cselect_b64 s[4:5], -1, 0
	s_and_b64 s[4:5], vcc, s[4:5]
	s_cmp_lt_i32 s21, s76
	s_waitcnt vmcnt(28)
	v_cndmask_b32_e64 v50, 0, v50, s[4:5]
	s_cselect_b64 s[4:5], -1, 0
	s_and_b64 s[4:5], vcc, s[4:5]
	s_cmp_lt_i32 s24, s76
	s_waitcnt vmcnt(27)
	v_cndmask_b32_e64 v49, 0, v49, s[4:5]
	s_cselect_b64 s[4:5], -1, 0
	s_and_b64 s[4:5], vcc, s[4:5]
	s_cmp_lt_i32 s25, s76
	s_waitcnt vmcnt(26)
	v_cndmask_b32_e64 v48, 0, v48, s[4:5]
	s_cselect_b64 s[4:5], -1, 0
	s_and_b64 s[4:5], vcc, s[4:5]
	s_cmp_lt_i32 s26, s76
	s_waitcnt vmcnt(25)
	v_cndmask_b32_e64 v47, 0, v47, s[4:5]
	s_cselect_b64 s[4:5], -1, 0
	s_and_b64 s[4:5], vcc, s[4:5]
	s_cmp_lt_i32 s27, s76
	s_waitcnt vmcnt(24)
; #define LAS __attribute__((address_space(3)))
; #define LDS_WAIT() asm volatile("s_waitcnt lgkmcnt(0)" ::: "memory")
; __device__ __forceinline__ void conv_load(const ConvItem& ci, int lane, float (&v)[64]) {
;     ...
;     for (int i = 0; i < 64; ++i) v[i] = (okc && (ci.k0 + i) < ci.Ksrc) ? v[i] : 0.f;
; }
; __device__ __forceinline__ void conv_store(const ConvItem& ci, LAS float* scr, int lane, const float (&v)[64]) {
;     const int c = lane & 7;
;     f32x4 s0 = {1.f, 1.f, 1.f, 1.f}, s1 = s0;
;     if (ci.ks) { const int kb = ci.k0 + 8 * c < ci.Ksrc - 8 ? ci.k0 + 8 * c : ci.Ksrc - 8; s0 = *(const f32x4*)(ci.ks + kb); s1 = *(const f32x4*)(ci.ks + kb + 4); }
; #pragma unroll
;     for (int i = 0; i < 64; ++i) scr[i * 65 + lane] = v[i];
;     LDS_WAIT(); asm volatile("" ::: "memory");
; #pragma unroll
;     for (int j = 0; j < 8; ++j) { const int n = (lane >> 3) + 8 * j; const LAS float* s = scr + (8 * c) * 65 + n;
	v_cndmask_b32_e64 v46, 0, v46, s[4:5]
	s_cselect_b64 s[4:5], -1, 0
	s_and_b64 s[4:5], vcc, s[4:5]
	s_cmp_lt_i32 s18, s76
	s_waitcnt vmcnt(23)
	v_cndmask_b32_e64 v61, 0, v61, s[4:5]
	s_cselect_b64 s[4:5], -1, 0
	s_and_b64 s[4:5], vcc, s[4:5]
	s_cmp_lt_i32 s19, s76
	s_waitcnt vmcnt(22)
	v_cndmask_b32_e64 v60, 0, v60, s[4:5]
	s_cselect_b64 s[4:5], -1, 0
	s_and_b64 s[4:5], vcc, s[4:5]
	s_cmp_lt_i32 s28, s76
	s_waitcnt vmcnt(21)
	v_cndmask_b32_e64 v59, 0, v59, s[4:5]
	s_cselect_b64 s[4:5], -1, 0
	s_and_b64 s[4:5], vcc, s[4:5]
	s_cmp_lt_i32 s29, s76
	s_waitcnt vmcnt(20)
	v_cndmask_b32_e64 v58, 0, v58, s[4:5]
	s_cselect_b64 s[4:5], -1, 0
	s_and_b64 s[4:5], vcc, s[4:5]
	s_cmp_lt_i32 s22, s76
	s_waitcnt vmcnt(19)
	v_cndmask_b32_e64 v57, 0, v57, s[4:5]
	s_cselect_b64 s[4:5], -1, 0
	s_and_b64 s[4:5], vcc, s[4:5]
	s_cmp_lt_i32 s23, s76
	s_waitcnt vmcnt(18)
	v_cndmask_b32_e64 v56, 0, v56, s[4:5]
	s_cselect_b64 s[4:5], -1, 0
	s_and_b64 s[4:5], vcc, s[4:5]
	s_cmp_lt_i32 s30, s76
	s_waitcnt vmcnt(17)
	v_cndmask_b32_e64 v55, 0, v55, s[4:5]
	s_cselect_b64 s[4:5], -1, 0
	s_and_b64 s[4:5], vcc, s[4:5]
	s_cmp_lt_i32 s31, s76
	s_waitcnt vmcnt(16)
	v_cndmask_b32_e64 v54, 0, v54, s[4:5]
	s_cselect_b64 s[4:5], -1, 0
	s_and_b64 s[4:5], vcc, s[4:5]
	s_cmp_lt_i32 s36, s76
	s_waitcnt vmcnt(15)
	v_cndmask_b32_e64 v70, 0, v70, s[4:5]
	s_cselect_b64 s[4:5], -1, 0
	s_and_b64 s[4:5], vcc, s[4:5]
	s_cmp_lt_i32 s37, s76
	s_waitcnt vmcnt(14)
	v_cndmask_b32_e64 v69, 0, v69, s[4:5]
	s_cselect_b64 s[4:5], -1, 0
	s_and_b64 s[4:5], vcc, s[4:5]
	s_cmp_lt_i32 s38, s76
	s_waitcnt vmcnt(13)
	v_cndmask_b32_e64 v68, 0, v68, s[4:5]
	s_cselect_b64 s[4:5], -1, 0
	s_and_b64 s[4:5], vcc, s[4:5]
	s_cmp_lt_i32 s39, s76
	s_waitcnt vmcnt(12)
	v_cndmask_b32_e64 v67, 0, v67, s[4:5]
	s_cselect_b64 s[4:5], -1, 0
	s_and_b64 s[4:5], vcc, s[4:5]
	s_cmp_lt_i32 s34, s76
	s_waitcnt vmcnt(11)
	v_cndmask_b32_e64 v66, 0, v66, s[4:5]
	s_cselect_b64 s[4:5], -1, 0
	s_and_b64 s[4:5], vcc, s[4:5]
	s_cmp_lt_i32 s35, s76
	s_waitcnt vmcnt(10)
	v_cndmask_b32_e64 v64, 0, v64, s[4:5]
	s_cselect_b64 s[4:5], -1, 0
	s_and_b64 s[4:5], vcc, s[4:5]
	s_cmp_lt_i32 s42, s76
	s_waitcnt vmcnt(9)
	v_cndmask_b32_e64 v63, 0, v63, s[4:5]
	s_cselect_b64 s[4:5], -1, 0
	s_and_b64 s[4:5], vcc, s[4:5]
	s_cmp_lt_i32 s43, s76
	s_waitcnt vmcnt(8)
	v_cndmask_b32_e64 v62, 0, v62, s[4:5]
	s_cselect_b64 s[4:5], -1, 0
	s_and_b64 s[4:5], vcc, s[4:5]
	s_cmp_lt_i32 s54, s76
	s_waitcnt vmcnt(7)
	v_cndmask_b32_e64 v65, 0, v65, s[4:5]
	s_cselect_b64 s[4:5], -1, 0
	s_and_b64 s[4:5], vcc, s[4:5]
	s_cmp_lt_i32 s55, s76
	s_waitcnt vmcnt(6)
	v_cndmask_b32_e64 v74, 0, v74, s[4:5]
	s_cselect_b64 s[4:5], -1, 0
	s_and_b64 s[4:5], vcc, s[4:5]
	s_cmp_lt_i32 s46, s76
	ds_write2_b32 v12, v21, v20 offset1:65
	ds_write2_b32 v12, v19, v18 offset0:130 offset1:195
	v_add_u32_e32 v18, 0x400, v12
	s_waitcnt vmcnt(5)
	v_cndmask_b32_e64 v73, 0, v73, s[4:5]
	s_cselect_b64 s[4:5], -1, 0
	ds_write2_b32 v18, v17, v16 offset0:4 offset1:69
	ds_write2_b32 v18, v15, v8 offset0:134 offset1:199
	v_add_u32_e32 v8, 0x800, v12
	s_and_b64 s[4:5], vcc, s[4:5]
	ds_write2_b32 v8, v29, v28 offset0:8 offset1:73
	ds_write2_b32 v8, v27, v26 offset0:138 offset1:203
	v_add_u32_e32 v8, 0xc00, v12
	s_cmp_lt_i32 s47, s76
	ds_write2_b32 v8, v25, v24 offset0:12 offset1:77
	ds_write2_b32 v8, v23, v22 offset0:142 offset1:207
	v_add_u32_e32 v8, 0x1000, v12
	s_waitcnt vmcnt(4)
	v_cndmask_b32_e64 v72, 0, v72, s[4:5]
	s_cselect_b64 s[4:5], -1, 0
	ds_write2_b32 v8, v37, v36 offset0:16 offset1:81
	ds_write2_b32 v8, v35, v34 offset0:146 offset1:211
	v_add_u32_e32 v8, 0x1400, v12
	s_and_b64 s[4:5], vcc, s[4:5]
	ds_write2_b32 v8, v33, v32 offset0:20 offset1:85
	ds_write2_b32 v8, v31, v30 offset0:150 offset1:215
	v_add_u32_e32 v8, 0x1800, v12
	s_cmp_lt_i32 s48, s76
	ds_write2_b32 v8, v45, v44 offset0:24 offset1:89
	ds_write2_b32 v8, v43, v42 offset0:154 offset1:219
	v_add_u32_e32 v8, 0x1c00, v12
	s_waitcnt vmcnt(3)
	v_cndmask_b32_e64 v71, 0, v71, s[4:5]
	s_cselect_b64 s[4:5], -1, 0
	ds_write2_b32 v8, v41, v40 offset0:28 offset1:93
	ds_write2_b32 v8, v39, v38 offset0:158 offset1:223
	v_add_u32_e32 v8, 0x2000, v12
	s_and_b64 s[4:5], vcc, s[4:5]
	ds_write2_b32 v8, v53, v52 offset0:32 offset1:97
	ds_write2_b32 v8, v51, v50 offset0:162 offset1:227
	v_add_u32_e32 v8, 0x2400, v12
	s_cmp_lt_i32 s49, s76
	ds_write2_b32 v8, v49, v48 offset0:36 offset1:101
	ds_write2_b32 v8, v47, v46 offset0:166 offset1:231
	v_add_u32_e32 v8, 0x2800, v12
	s_waitcnt vmcnt(2)
	v_cndmask_b32_e64 v77, 0, v77, s[4:5]
	s_cselect_b64 s[4:5], -1, 0
	ds_write2_b32 v8, v61, v60 offset0:40 offset1:105
	ds_write2_b32 v8, v59, v58 offset0:170 offset1:235
	v_add_u32_e32 v8, 0x2c00, v12
	s_and_b64 s[4:5], vcc, s[4:5]
	ds_write2_b32 v8, v57, v56 offset0:44 offset1:109
	ds_write2_b32 v8, v55, v54 offset0:174 offset1:239
	v_add_u32_e32 v8, 0x3000, v12
	s_cmp_lt_i32 s44, s76
	ds_write2_b32 v8, v70, v69 offset0:48 offset1:113
	ds_write2_b32 v8, v68, v67 offset0:178 offset1:243
	v_add_u32_e32 v8, 0x3400, v12
	s_waitcnt vmcnt(1)
	v_cndmask_b32_e64 v76, 0, v76, s[4:5]
	s_cselect_b64 s[4:5], -1, 0
	ds_write2_b32 v8, v66, v64 offset0:52 offset1:117
	ds_write2_b32 v8, v63, v62 offset0:182 offset1:247
	v_add_u32_e32 v8, 0x3800, v12
	s_and_b64 vcc, vcc, s[4:5]
	ds_write2_b32 v8, v65, v74 offset0:56 offset1:121
	ds_write2_b32 v8, v73, v72 offset0:186 offset1:251
	v_add_u32_e32 v8, 0x3c00, v12
	s_waitcnt vmcnt(0)
	v_cndmask_b32_e32 v75, 0, v75, vcc
	ds_write2_b32 v8, v71, v77 offset0:60 offset1:125
	ds_write2_b32 v8, v76, v75 offset0:190 offset1:255
	s_waitcnt lgkmcnt(0)
	ds_read2_b32 v[16:17], v14 offset1:65
	v_add_u32_e32 v24, s59, v13
	v_mul_lo_u32 v22, s57, v24
	s_ashr_i32 s59, s58, 31
	v_readlane_b32 s76, v254, 31
	s_waitcnt lgkmcnt(0)
; __device__ __forceinline__ unsigned cvt_pk_bf16(float lo, float hi) { unsigned r; asm volatile("v_cvt_pk_bf16_f32 %0, %1, %2" : "=v"(r) : "v"(lo), "v"(hi)); return r; }
; #define LAS __attribute__((address_space(3)))
; __device__ __forceinline__ void conv_store(const ConvItem& ci, LAS float* scr, int lane, const float (&v)[64]) {
;     ...
;     for (int j = 0; j < 8; ++j) { const int n = (lane >> 3) + 8 * j; const LAS float* s = scr + (8 * c) * 65 + n;
;         v4u o; o.x = cvt_pk_bf16(s[0 * 65] * s0[0], s[1 * 65] * s0[1]); o.y = cvt_pk_bf16(s[2 * 65] * s0[2], s[3 * 65] * s0[3]); o.z = cvt_pk_bf16(s[4 * 65] * s1[0], s[5 * 65] * s1[1]); o.w = cvt_pk_bf16(s[6 * 65] * s1[2], s[7 * 65] * s1[3]);
;         *(v4u*)(ci.dst + (size_t)(ci.drow0 + n) * ci.ldd + ci.k0 + 8 * c) = o; }
	v_mul_f32_e32 v8, v4, v16
	v_mul_f32_e32 v15, v5, v17
	v_cvt_pk_bf16_f32 v16, v8, v15
	ds_read2_b32 v[18:19], v14 offset0:130 offset1:195
	s_add_i32 s3, s3, s33
	s_add_i32 s66, s66, s67
	s_add_i32 s68, s68, s69
	s_add_i32 s70, s70, s71
	s_waitcnt lgkmcnt(0)
	v_mul_f32_e32 v15, v7, v19
	v_mul_f32_e32 v8, v6, v18
	v_cvt_pk_bf16_f32 v17, v8, v15
	v_add_u32_e32 v15, 0x400, v14
	ds_read2_b32 v[18:19], v15 offset0:4 offset1:69
	s_add_i32 s72, s72, s73
	s_add_i32 s74, s74, s75
	v_readlane_b32 s78, v254, 33
	v_readlane_b32 s79, v254, 34
	s_waitcnt lgkmcnt(0)
	v_mul_f32_e32 v8, v0, v18
	v_mul_f32_e32 v18, v1, v19
	v_cvt_pk_bf16_f32 v18, v8, v18
	ds_read2_b32 v[20:21], v15 offset0:134 offset1:199
	v_readlane_b32 s80, v255, 21
	v_readlane_b32 s77, v254, 32
	s_movk_i32 s78, 0x1580
	v_readlane_b32 s82, v255, 23
	s_waitcnt lgkmcnt(0)
	v_mul_f32_e32 v8, v2, v20
	v_mul_f32_e32 v19, v3, v21
	v_cvt_pk_bf16_f32 v19, v8, v19
	v_ashrrev_i32_e32 v8, 31, v24
	v_mul_lo_u32 v8, s56, v8
	v_mad_u64_u32 v[20:21], s[4:5], s56, v24, 0
	v_add3_u32 v21, v21, v8, v22
	ds_read2_b32 v[22:23], v14 offset0:8 offset1:73
	v_lshl_add_u64 v[20:21], v[20:21], 1, s[60:61]
	s_lshl_b64 s[4:5], s[58:59], 1
	v_lshl_add_u64 v[20:21], v[20:21], 0, s[4:5]
	v_lshlrev_b32_e32 v8, 1, v10
	v_lshl_add_u64 v[20:21], v[20:21], 0, v[8:9]
	global_store_dwordx4 v[20:21], v[16:19], off
	s_cmpk_lt_i32 s3, 24192
	v_readlane_b32 s83, v255, 24
	s_waitcnt lgkmcnt(0)
	v_mul_f32_e32 v16, v4, v22
	v_mul_f32_e32 v17, v5, v23
	v_cvt_pk_bf16_f32 v16, v16, v17
	ds_read2_b32 v[18:19], v14 offset0:138 offset1:203
	s_mov_b32 s79, 0x3f22f983
	s_mov_b32 s85, 0xbfc90fda
	s_brev_b32 s86, 1
	s_movk_i32 s87, 0x1f8
	s_waitcnt lgkmcnt(0)
	v_mul_f32_e32 v17, v6, v18
	v_mul_f32_e32 v18, v7, v19
	v_cvt_pk_bf16_f32 v17, v17, v18
	ds_read2_b32 v[18:19], v15 offset0:12 offset1:77
	s_mov_b64 s[88:89], 0x80
	s_mov_b64 s[92:93], 0x4000
	s_mov_b64 s[94:95], 0x4800
	v_readlane_b32 s81, v255, 22
	s_waitcnt lgkmcnt(0)
	v_mul_f32_e32 v18, v0, v18
	v_mul_f32_e32 v19, v1, v19
	v_cvt_pk_bf16_f32 v18, v18, v19
	ds_read2_b32 v[20:21], v15 offset0:142 offset1:207
	s_waitcnt lgkmcnt(0)
	v_mul_f32_e32 v19, v2, v20
	v_mul_f32_e32 v20, v3, v21
	v_cvt_pk_bf16_f32 v19, v19, v20
	v_add_u32_e32 v20, 8, v24
	v_ashrrev_i32_e32 v21, 31, v20
	v_mul_lo_u32 v22, s56, v21
	v_mul_lo_u32 v23, s57, v20
	v_mad_u64_u32 v[20:21], s[6:7], s56, v20, 0
	v_add3_u32 v21, v21, v22, v23
	ds_read2_b32 v[22:23], v14 offset0:16 offset1:81
	v_lshl_add_u64 v[20:21], v[20:21], 1, s[60:61]
	v_lshl_add_u64 v[20:21], v[20:21], 0, s[4:5]
	v_lshl_add_u64 v[20:21], v[20:21], 0, v[8:9]
	global_store_dwordx4 v[20:21], v[16:19], off
	s_waitcnt lgkmcnt(0)
	s_nop 0
	v_mul_f32_e32 v16, v4, v22
	v_mul_f32_e32 v17, v5, v23
	v_cvt_pk_bf16_f32 v16, v16, v17
	ds_read2_b32 v[18:19], v14 offset0:146 offset1:211
	s_waitcnt lgkmcnt(0)
	v_mul_f32_e32 v17, v6, v18
	v_mul_f32_e32 v18, v7, v19
	v_cvt_pk_bf16_f32 v17, v17, v18
	ds_read2_b32 v[18:19], v15 offset0:20 offset1:85
	s_waitcnt lgkmcnt(0)
	v_mul_f32_e32 v18, v0, v18
	v_mul_f32_e32 v19, v1, v19
	v_cvt_pk_bf16_f32 v18, v18, v19
	ds_read2_b32 v[20:21], v15 offset0:150 offset1:215
	s_waitcnt lgkmcnt(0)
	v_mul_f32_e32 v19, v2, v20
	v_mul_f32_e32 v20, v3, v21
	v_cvt_pk_bf16_f32 v19, v19, v20
	v_add_u32_e32 v20, 16, v24
	v_ashrrev_i32_e32 v21, 31, v20
	v_mul_lo_u32 v22, s56, v21
	v_mul_lo_u32 v23, s57, v20
	v_mad_u64_u32 v[20:21], s[6:7], s56, v20, 0
	v_add3_u32 v21, v21, v22, v23
	ds_read2_b32 v[22:23], v14 offset0:24 offset1:89
	v_lshl_add_u64 v[20:21], v[20:21], 1, s[60:61]
	v_lshl_add_u64 v[20:21], v[20:21], 0, s[4:5]
	v_lshl_add_u64 v[20:21], v[20:21], 0, v[8:9]
	global_store_dwordx4 v[20:21], v[16:19], off
	s_waitcnt lgkmcnt(0)
	s_nop 0
	v_mul_f32_e32 v16, v4, v22
	v_mul_f32_e32 v17, v5, v23
	v_cvt_pk_bf16_f32 v16, v16, v17
	ds_read2_b32 v[18:19], v14 offset0:154 offset1:219
	s_waitcnt lgkmcnt(0)
	v_mul_f32_e32 v17, v6, v18
	v_mul_f32_e32 v18, v7, v19
	v_cvt_pk_bf16_f32 v17, v17, v18
	ds_read2_b32 v[18:19], v15 offset0:28 offset1:93
	s_waitcnt lgkmcnt(0)
	v_mul_f32_e32 v18, v0, v18
	v_mul_f32_e32 v19, v1, v19
	v_cvt_pk_bf16_f32 v18, v18, v19
	ds_read2_b32 v[20:21], v15 offset0:158 offset1:223
	s_waitcnt lgkmcnt(0)
; __device__ __forceinline__ unsigned cvt_pk_bf16(float lo, float hi) { unsigned r; asm volatile("v_cvt_pk_bf16_f32 %0, %1, %2" : "=v"(r) : "v"(lo), "v"(hi)); return r; }
; #define LAS __attribute__((address_space(3)))
; #define LDS_WAIT() asm volatile("s_waitcnt lgkmcnt(0)" ::: "memory")
; __device__ __forceinline__ void conv_store(const ConvItem& ci, LAS float* scr, int lane, const float (&v)[64]) {
;     ...
;     for (int j = 0; j < 8; ++j) { const int n = (lane >> 3) + 8 * j; const LAS float* s = scr + (8 * c) * 65 + n;
;         v4u o; o.x = cvt_pk_bf16(s[0 * 65] * s0[0], s[1 * 65] * s0[1]); o.y = cvt_pk_bf16(s[2 * 65] * s0[2], s[3 * 65] * s0[3]); o.z = cvt_pk_bf16(s[4 * 65] * s1[0], s[5 * 65] * s1[1]); o.w = cvt_pk_bf16(s[6 * 65] * s1[2], s[7 * 65] * s1[3]);
;         *(v4u*)(ci.dst + (size_t)(ci.drow0 + n) * ci.ldd + ci.k0 + 8 * c) = o; }
;     LDS_WAIT(); asm volatile("" ::: "memory");
; }
	v_mul_f32_e32 v19, v2, v20
	v_mul_f32_e32 v20, v3, v21
	v_cvt_pk_bf16_f32 v19, v19, v20
	v_add_u32_e32 v20, 24, v24
	v_ashrrev_i32_e32 v21, 31, v20
	v_mul_lo_u32 v22, s56, v21
	v_mul_lo_u32 v23, s57, v20
	v_mad_u64_u32 v[20:21], s[6:7], s56, v20, 0
	v_add3_u32 v21, v21, v22, v23
	ds_read2_b32 v[22:23], v14 offset0:32 offset1:97
	v_lshl_add_u64 v[20:21], v[20:21], 1, s[60:61]
	v_lshl_add_u64 v[20:21], v[20:21], 0, s[4:5]
	v_lshl_add_u64 v[20:21], v[20:21], 0, v[8:9]
	global_store_dwordx4 v[20:21], v[16:19], off
	s_waitcnt lgkmcnt(0)
	s_nop 0
	v_mul_f32_e32 v16, v4, v22
	v_mul_f32_e32 v17, v5, v23
	v_cvt_pk_bf16_f32 v16, v16, v17
	ds_read2_b32 v[18:19], v14 offset0:162 offset1:227
	s_waitcnt lgkmcnt(0)
	v_mul_f32_e32 v17, v6, v18
	v_mul_f32_e32 v18, v7, v19
	v_cvt_pk_bf16_f32 v17, v17, v18
	ds_read2_b32 v[18:19], v15 offset0:36 offset1:101
	s_waitcnt lgkmcnt(0)
	v_mul_f32_e32 v18, v0, v18
	v_mul_f32_e32 v19, v1, v19
	v_cvt_pk_bf16_f32 v18, v18, v19
	ds_read2_b32 v[20:21], v15 offset0:166 offset1:231
	s_waitcnt lgkmcnt(0)
	v_mul_f32_e32 v19, v2, v20
	v_mul_f32_e32 v20, v3, v21
	v_cvt_pk_bf16_f32 v19, v19, v20
	v_add_u32_e32 v20, 32, v24
	v_ashrrev_i32_e32 v21, 31, v20
	v_mul_lo_u32 v22, s56, v21
	v_mul_lo_u32 v23, s57, v20
	v_mad_u64_u32 v[20:21], s[6:7], s56, v20, 0
	v_add3_u32 v21, v21, v22, v23
	ds_read2_b32 v[22:23], v14 offset0:40 offset1:105
	v_lshl_add_u64 v[20:21], v[20:21], 1, s[60:61]
	v_lshl_add_u64 v[20:21], v[20:21], 0, s[4:5]
	v_lshl_add_u64 v[20:21], v[20:21], 0, v[8:9]
	global_store_dwordx4 v[20:21], v[16:19], off
	s_waitcnt lgkmcnt(0)
	s_nop 0
	v_mul_f32_e32 v16, v4, v22
	v_mul_f32_e32 v17, v5, v23
	v_cvt_pk_bf16_f32 v16, v16, v17
	ds_read2_b32 v[18:19], v14 offset0:170 offset1:235
	s_waitcnt lgkmcnt(0)
	v_mul_f32_e32 v17, v6, v18
	v_mul_f32_e32 v18, v7, v19
	v_cvt_pk_bf16_f32 v17, v17, v18
	ds_read2_b32 v[18:19], v15 offset0:44 offset1:109
	s_waitcnt lgkmcnt(0)
	v_mul_f32_e32 v18, v0, v18
	v_mul_f32_e32 v19, v1, v19
	v_cvt_pk_bf16_f32 v18, v18, v19
	ds_read2_b32 v[20:21], v15 offset0:174 offset1:239
	s_waitcnt lgkmcnt(0)
	v_mul_f32_e32 v19, v2, v20
	v_mul_f32_e32 v20, v3, v21
	v_cvt_pk_bf16_f32 v19, v19, v20
	v_add_u32_e32 v20, 40, v24
	v_ashrrev_i32_e32 v21, 31, v20
	v_mul_lo_u32 v22, s56, v21
	v_mul_lo_u32 v23, s57, v20
	v_mad_u64_u32 v[20:21], s[6:7], s56, v20, 0
	v_add3_u32 v21, v21, v22, v23
	ds_read2_b32 v[22:23], v14 offset0:48 offset1:113
	v_lshl_add_u64 v[20:21], v[20:21], 1, s[60:61]
	v_lshl_add_u64 v[20:21], v[20:21], 0, s[4:5]
	v_lshl_add_u64 v[20:21], v[20:21], 0, v[8:9]
	global_store_dwordx4 v[20:21], v[16:19], off
	s_waitcnt lgkmcnt(0)
	s_nop 0
	v_mul_f32_e32 v16, v4, v22
	v_mul_f32_e32 v17, v5, v23
	v_cvt_pk_bf16_f32 v16, v16, v17
	ds_read2_b32 v[18:19], v14 offset0:178 offset1:243
	s_waitcnt lgkmcnt(0)
	v_mul_f32_e32 v17, v6, v18
	v_mul_f32_e32 v18, v7, v19
	v_cvt_pk_bf16_f32 v17, v17, v18
	ds_read2_b32 v[18:19], v15 offset0:52 offset1:117
	s_waitcnt lgkmcnt(0)
	v_mul_f32_e32 v18, v0, v18
	v_mul_f32_e32 v19, v1, v19
	v_cvt_pk_bf16_f32 v18, v18, v19
	ds_read2_b32 v[20:21], v15 offset0:182 offset1:247
	s_waitcnt lgkmcnt(0)
	v_mul_f32_e32 v19, v2, v20
	v_mul_f32_e32 v20, v3, v21
	v_cvt_pk_bf16_f32 v19, v19, v20
	v_add_u32_e32 v20, 48, v24
	v_ashrrev_i32_e32 v21, 31, v20
	v_mul_lo_u32 v22, s56, v21
	v_mul_lo_u32 v23, s57, v20
	v_mad_u64_u32 v[20:21], s[6:7], s56, v20, 0
	v_add3_u32 v21, v21, v22, v23
	ds_read2_b32 v[22:23], v14 offset0:56 offset1:121
	v_lshl_add_u64 v[20:21], v[20:21], 1, s[60:61]
	v_lshl_add_u64 v[20:21], v[20:21], 0, s[4:5]
	v_lshl_add_u64 v[20:21], v[20:21], 0, v[8:9]
	global_store_dwordx4 v[20:21], v[16:19], off
	s_waitcnt lgkmcnt(0)
	v_mul_f32_e32 v4, v4, v22
	v_mul_f32_e32 v5, v5, v23
	v_cvt_pk_bf16_f32 v4, v4, v5
	ds_read2_b32 v[16:17], v14 offset0:186 offset1:251
	s_waitcnt lgkmcnt(0)
	v_mul_f32_e32 v5, v6, v16
	v_mul_f32_e32 v6, v7, v17
	v_cvt_pk_bf16_f32 v5, v5, v6
	ds_read2_b32 v[6:7], v15 offset0:60 offset1:125
	s_waitcnt lgkmcnt(0)
	v_mul_f32_e32 v0, v0, v6
	v_mul_f32_e32 v1, v1, v7
	v_cvt_pk_bf16_f32 v6, v0, v1
	ds_read2_b32 v[0:1], v15 offset0:190 offset1:255
	s_waitcnt lgkmcnt(0)
	v_mul_f32_e32 v0, v2, v0
	v_mul_f32_e32 v1, v3, v1
	v_cvt_pk_bf16_f32 v7, v0, v1
	v_add_u32_e32 v0, 56, v24
	v_ashrrev_i32_e32 v1, 31, v0
	v_mul_lo_u32 v2, s56, v1
	v_mul_lo_u32 v3, s57, v0
	v_mad_u64_u32 v[0:1], s[6:7], s56, v0, 0
	v_add3_u32 v1, v1, v2, v3
	v_lshl_add_u64 v[0:1], v[0:1], 1, s[60:61]
	v_lshl_add_u64 v[0:1], v[0:1], 0, s[4:5]
	v_lshl_add_u64 v[0:1], v[0:1], 0, v[8:9]
	global_store_dwordx4 v[0:1], v[4:7], off
	s_waitcnt lgkmcnt(0)
	s_cbranch_scc0 .Lcvp31_ret

; #define LAS __attribute__((address_space(3)))
; __global__ void __launch_bounds__(NWAVES * 64, 2) mk_fwd(Args args) {
;     ...
;             PH_LOCALS
;             LAS float* scr = (LAS float*)(lds + RING_OFF + wave * 16640);   static_assert(8 * 16640 <= LDSCTL_OFF, "converter scratch below the LDS control words");
;             constexpr int I_UP = (D / 64) * (NUP / 64), I_DN = (DFF / 64) * (D / 64), I_IN = (D / 64) * (DINP / 64), I_GLU = 16 * 16, I_L = 4 * 16, I_V1 = 16 * 4, I_V2 = 4 * 16,
;                           I_BS5 = 16 * 32, I_BAT = 8 * 32, I_BRW = 16 * 32, I_OUT = 32 * 32;
;             constexpr int NITEMS = 2 * I_UP + 2 * I_DN + I_IN + I_GLU + 3 * I_L + I_V1 + I_V2 + I_BS5 + I_BAT + I_BRW + I_OUT;
;             const int lv = l > 0 ? l - 1 : 0;
;     ...
;             for (int it = gw; it < NITEMS; it += NGW) {
;                 ConvItem ca; CONV_DESC(ca, it);
.Lcvp31_ret:
.Lcvrs_p31:
	v_readlane_b32 s98, v254, 38
	s_nop 3
	s_cmp_gt_u32 s98, 2
	s_cbranch_scc1 .Lcvrs_p32
	v_readlane_b32 s0, v254, 8
	v_readlane_b32 s4, v254, 10
	v_readlane_b32 s1, v254, 9
	v_mbcnt_lo_u32_b32 v11, -1, 0
	v_mbcnt_hi_u32_b32 v11, -1, v11
	s_load_dword s6, s[0:1], 0x0
	s_mov_b32 s3, s84
	s_waitcnt lgkmcnt(0)
	s_movk_i32 s6, 128
	s_lshl_b32 s3, s3, 3
	v_readlane_b32 s0, v254, 0
	s_add_i32 s3, s3, s4
	s_add_i32 s3, s3, 0xfffffc00
	v_readlane_b32 s1, v254, 1
	s_cmpk_gt_i32 s3, 5503
	s_cbranch_scc1 .Lcvp32_ret
	s_load_dwordx2 s[8:9], s[0:1], 0x138
	v_readlane_b32 s14, v254, 38
	s_nop 0
	s_add_i32 s14, s14, 1
	s_mulk_i32 s4, 0x4100
	s_add_i32 s7, s4, 0
	v_sub_u32_e64 v0, s14, 1 clamp
	s_lshl_b32 s33, s6, 3
	v_readfirstlane_b32 s4, v0
	s_lshl_b32 s96, s4, 16
	s_waitcnt lgkmcnt(0)
	s_add_u32 s4, s8, 0x22800000
	s_addc_u32 s5, s9, 0
	v_writelane_b32 v254, s4, 39
	s_mov_b32 s15, s97
	v_and_b32_e32 v0, 7, v11
	v_writelane_b32 v254, s5, 40
	s_add_u32 s4, s8, 0x22780000
	s_addc_u32 s5, s9, 0
	v_writelane_b32 v254, s4, 41
	v_ashrrev_i32_e32 v13, 3, v11
	v_lshlrev_b32_e32 v10, 3, v0
	v_writelane_b32 v254, s5, 42
	s_lshl_b32 s4, s14, 18
	s_add_u32 s10, s8, 0x22700000
	s_addc_u32 s11, s9, 0
	v_writelane_b32 v254, s10, 43
	s_mov_b32 s5, s97
	v_mul_u32_u24_e32 v0, 0x820, v0
	v_writelane_b32 v254, s11, 44
	s_mul_i32 s10, s14, 0x18000
	s_mov_b32 s11, s97
	v_writelane_b32 v254, s10, 45
	v_lshlrev_b32_e32 v1, 2, v13
	v_lshl_add_u32 v12, v11, 2, s7
	v_writelane_b32 v254, s11, 46
	s_add_u32 s10, s8, 0x22680000
	s_addc_u32 s11, s9, 0
	v_writelane_b32 v254, s10, 47
	v_add3_u32 v14, s7, v0, v1
	s_mov_b32 s41, s97
	v_writelane_b32 v254, s11, 48
	s_add_u32 s10, s8, 0x22600000
	s_addc_u32 s11, s9, 0
	v_writelane_b32 v254, s10, 49
	s_nop 1
	v_writelane_b32 v254, s11, 50
	s_lshl_b32 s10, s14, 20
	s_mov_b32 s11, s97
	v_writelane_b32 v254, s10, 51
	s_nop 1
	v_writelane_b32 v254, s11, 52
	s_add_u32 s10, s8, 0x22400000
	s_addc_u32 s11, s9, 0
	v_writelane_b32 v254, s10, 53
	s_nop 1
	v_writelane_b32 v254, s11, 54
	s_lshl_b32 s10, s14, 21
	s_mov_b32 s11, s97
	v_writelane_b32 v254, s10, 55
	s_nop 1
	v_writelane_b32 v254, s11, 56
	s_add_u32 s10, s8, 0x22e80000
	s_addc_u32 s11, s9, 0
	v_writelane_b32 v254, s10, 57
	s_nop 1
	v_writelane_b32 v254, s11, 58
	s_add_u32 s10, s8, 0x27b80000
	s_addc_u32 s11, s9, 0
	v_writelane_b32 v254, s10, 59
	s_nop 1
	v_writelane_b32 v254, s11, 60
	s_add_u32 s10, s8, 0x22880000
	s_addc_u32 s11, s9, 0
	v_writelane_b32 v254, s10, 61
	s_nop 1
	v_writelane_b32 v254, s11, 62
	s_lshl_b32 s10, s14, 22
	s_add_u32 s12, s8, 0x23280000
	s_addc_u32 s13, s9, 0
	v_writelane_b32 v254, s12, 63
	s_mov_b32 s11, s97
	s_nop 0
	v_writelane_b32 v255, s13, 0
	s_mul_i32 s12, s14, 0xac0000
	s_mov_b32 s13, s97
	v_writelane_b32 v255, s12, 1
	s_nop 1
	v_writelane_b32 v255, s13, 2
	s_add_u32 s12, s8, 0x26580000
	s_addc_u32 s13, s9, 0
	v_writelane_b32 v255, s12, 3
	s_nop 1
	v_writelane_b32 v255, s13, 4
	s_add_u32 s12, s8, 0x1d200000
	s_addc_u32 s13, s9, 0
	s_lshl_b32 s40, s14, 11
	v_writelane_b32 v255, s12, 5
	s_add_u32 s16, s8, 0x1e800000
	s_addc_u32 s17, s9, 0
	v_writelane_b32 v255, s13, 6
	v_writelane_b32 v255, s16, 7
	s_mul_i32 s12, s14, 0x1de0000
	s_mul_i32 s14, s14, 0x1580000
	v_writelane_b32 v255, s17, 8
	v_writelane_b32 v255, s14, 9
	s_mov_b32 s13, s97
	s_nop 0
	v_writelane_b32 v255, s15, 10
	s_add_u32 s14, s8, 0x23a80000
	s_addc_u32 s15, s9, 0
	v_writelane_b32 v255, s14, 11
	s_add_u32 s8, s8, 0x1a700000
	s_addc_u32 s9, s9, 0
	v_writelane_b32 v255, s15, 12
	v_writelane_b32 v255, s8, 13
	s_lshl_b64 s[4:5], s[4:5], 2
	s_lshl_b32 s7, s3, 4
	v_writelane_b32 v255, s9, 14
	v_writelane_b32 v255, s4, 15
	s_add_i32 s72, s7, 0xc00
	s_lshl_b32 s7, s3, 1
	v_writelane_b32 v255, s5, 16
	s_lshl_b64 s[4:5], s[10:11], 2
	v_writelane_b32 v255, s4, 17
	s_lshl_b32 s66, s3, 6
	s_lshl_b32 s67, s6, 9
	v_writelane_b32 v255, s5, 18
	s_lshl_b64 s[4:5], s[12:13], 2
	v_writelane_b32 v255, s4, 19
	s_lshl_b32 s68, s3, 5
	s_lshl_b32 s69, s6, 8
	v_writelane_b32 v255, s5, 20
	v_writelane_b32 v255, s80, 21
	s_lshl_b32 s70, s3, 2
	s_lshl_b32 s71, s6, 5
	v_writelane_b32 v255, s81, 22
	v_writelane_b32 v255, s82, 23
	s_lshl_b32 s73, s6, 7
	s_add_i32 s74, s7, 0x13500
	s_lshl_b32 s75, s6, 4
	v_writelane_b32 v255, s83, 24
	s_branch .Lcvp32_31

; #define LAS __attribute__((address_space(3)))
; __global__ void __launch_bounds__(NWAVES * 64, 2) mk_fwd(Args args) {
;     ...
;             PH_LOCALS
;             LAS float* scr = (LAS float*)(lds + RING_OFF + wave * 16640);   static_assert(8 * 16640 <= LDSCTL_OFF, "converter scratch below the LDS control words");
;             constexpr int I_UP = (D / 64) * (NUP / 64), I_DN = (DFF / 64) * (D / 64), I_IN = (D / 64) * (DINP / 64), I_GLU = 16 * 16, I_L = 4 * 16, I_V1 = 16 * 4, I_V2 = 4 * 16,
;                           I_BS5 = 16 * 32, I_BAT = 8 * 32, I_BRW = 16 * 32, I_OUT = 32 * 32;
;             constexpr int NITEMS = 2 * I_UP + 2 * I_DN + I_IN + I_GLU + 3 * I_L + I_V1 + I_V2 + I_BS5 + I_BAT + I_BRW + I_OUT;
;             const int lv = l > 0 ? l - 1 : 0;
;     ...
;             for (int it = gw; it < NITEMS; it += NGW) {
;                 ConvItem ca; CONV_DESC(ca, it);
.Lcvp130_ret:
.Lcvrs_p130:
	v_readlane_b32 s0, v254, 8
	v_readlane_b32 s4, v254, 10
	v_readlane_b32 s1, v254, 9
	v_mbcnt_lo_u32_b32 v11, -1, 0
	v_mbcnt_hi_u32_b32 v11, -1, v11
	s_load_dword s6, s[0:1], 0x0
	s_mov_b32 s3, s84
	s_waitcnt lgkmcnt(0)
	s_movk_i32 s6, 160
	s_lshl_b32 s3, s3, 3
	v_readlane_b32 s0, v254, 0
	s_add_i32 s3, s3, s4
	s_add_i32 s3, s3, 0x6480
	v_readlane_b32 s1, v254, 1
	s_cmpk_gt_i32 s3, 27071
	s_cbranch_scc1 .Lcvp131_ret
	s_load_dwordx2 s[8:9], s[0:1], 0x138
	v_readlane_b32 s14, v254, 38
	s_nop 0
	s_add_i32 s14, s14, 1
	s_mulk_i32 s4, 0x4100
	s_add_i32 s7, s4, 0
	v_sub_u32_e64 v0, s14, 1 clamp
	s_lshl_b32 s33, s6, 3
	v_readfirstlane_b32 s4, v0
	s_lshl_b32 s96, s4, 16
	s_waitcnt lgkmcnt(0)
	s_add_u32 s4, s8, 0x22800000
	s_addc_u32 s5, s9, 0
	v_writelane_b32 v254, s4, 39
	s_mov_b32 s15, s97
	v_and_b32_e32 v0, 7, v11
	v_writelane_b32 v254, s5, 40
	s_add_u32 s4, s8, 0x22780000
	s_addc_u32 s5, s9, 0
	v_writelane_b32 v254, s4, 41
	v_ashrrev_i32_e32 v13, 3, v11
	v_lshlrev_b32_e32 v10, 3, v0
	v_writelane_b32 v254, s5, 42
	s_lshl_b32 s4, s14, 18
	s_add_u32 s10, s8, 0x22700000
	s_addc_u32 s11, s9, 0
	v_writelane_b32 v254, s10, 43
	s_mov_b32 s5, s97
	v_mul_u32_u24_e32 v0, 0x820, v0
	v_writelane_b32 v254, s11, 44
	s_mul_i32 s10, s14, 0x18000
	s_mov_b32 s11, s97
	v_writelane_b32 v254, s10, 45
	v_lshlrev_b32_e32 v1, 2, v13
	v_lshl_add_u32 v12, v11, 2, s7
	v_writelane_b32 v254, s11, 46
	s_add_u32 s10, s8, 0x22680000
	s_addc_u32 s11, s9, 0
	v_writelane_b32 v254, s10, 47
	v_add3_u32 v14, s7, v0, v1
	s_mov_b32 s41, s97
	v_writelane_b32 v254, s11, 48
	s_add_u32 s10, s8, 0x22600000
	s_addc_u32 s11, s9, 0
	v_writelane_b32 v254, s10, 49
	s_nop 1
	v_writelane_b32 v254, s11, 50
	s_lshl_b32 s10, s14, 20
	s_mov_b32 s11, s97
	v_writelane_b32 v254, s10, 51
	s_nop 1
	v_writelane_b32 v254, s11, 52
	s_add_u32 s10, s8, 0x22400000
	s_addc_u32 s11, s9, 0
	v_writelane_b32 v254, s10, 53
	s_nop 1
	v_writelane_b32 v254, s11, 54
	s_lshl_b32 s10, s14, 21
	s_mov_b32 s11, s97
	v_writelane_b32 v254, s10, 55
	s_nop 1
	v_writelane_b32 v254, s11, 56
	s_add_u32 s10, s8, 0x22e80000
	s_addc_u32 s11, s9, 0
	v_writelane_b32 v254, s10, 57
	s_nop 1
	v_writelane_b32 v254, s11, 58
	s_add_u32 s10, s8, 0x27b80000
	s_addc_u32 s11, s9, 0
	v_writelane_b32 v254, s10, 59
	s_nop 1
	v_writelane_b32 v254, s11, 60
	s_add_u32 s10, s8, 0x22880000
	s_addc_u32 s11, s9, 0
	v_writelane_b32 v254, s10, 61
	s_nop 1
	v_writelane_b32 v254, s11, 62
	s_lshl_b32 s10, s14, 22
	s_add_u32 s12, s8, 0x23280000
	s_addc_u32 s13, s9, 0
	v_writelane_b32 v254, s12, 63
	s_mov_b32 s11, s97
	s_nop 0
	v_writelane_b32 v255, s13, 0
	s_mul_i32 s12, s14, 0xac0000
	s_mov_b32 s13, s97
	v_writelane_b32 v255, s12, 1
	s_nop 1
	v_writelane_b32 v255, s13, 2
	s_add_u32 s12, s8, 0x26580000
	s_addc_u32 s13, s9, 0
	v_writelane_b32 v255, s12, 3
	s_nop 1
	v_writelane_b32 v255, s13, 4
	s_add_u32 s12, s8, 0x1d200000
	s_addc_u32 s13, s9, 0
	s_lshl_b32 s40, s14, 11
	v_writelane_b32 v255, s12, 5
	s_add_u32 s16, s8, 0x1e800000
	s_addc_u32 s17, s9, 0
	v_writelane_b32 v255, s13, 6
	v_writelane_b32 v255, s16, 7
	s_mul_i32 s12, s14, 0x1de0000
	s_mul_i32 s14, s14, 0x1580000
	v_writelane_b32 v255, s17, 8
	v_writelane_b32 v255, s14, 9
	s_mov_b32 s13, s97
	s_nop 0
	v_writelane_b32 v255, s15, 10
	s_add_u32 s14, s8, 0x23a80000
	s_addc_u32 s15, s9, 0
	v_writelane_b32 v255, s14, 11
	s_add_u32 s8, s8, 0x1a700000
	s_addc_u32 s9, s9, 0
	v_writelane_b32 v255, s15, 12
	v_writelane_b32 v255, s8, 13
	s_lshl_b64 s[4:5], s[4:5], 2
	s_lshl_b32 s7, s3, 4
	v_writelane_b32 v255, s9, 14
	v_writelane_b32 v255, s4, 15
	s_add_i32 s72, s7, 0xc00
	s_lshl_b32 s7, s3, 1
	v_writelane_b32 v255, s5, 16
	s_lshl_b64 s[4:5], s[10:11], 2
	v_writelane_b32 v255, s4, 17
	s_lshl_b32 s66, s3, 6
	s_lshl_b32 s67, s6, 9
	v_writelane_b32 v255, s5, 18
	s_lshl_b64 s[4:5], s[12:13], 2
	v_writelane_b32 v255, s4, 19
	s_lshl_b32 s68, s3, 5
	s_lshl_b32 s69, s6, 8
	v_writelane_b32 v255, s5, 20
	v_writelane_b32 v255, s80, 21
	s_lshl_b32 s70, s3, 2
	s_lshl_b32 s71, s6, 5
	v_writelane_b32 v255, s81, 22
	v_writelane_b32 v255, s82, 23
	s_lshl_b32 s73, s6, 7
	s_add_i32 s74, s7, 0x13500
	s_lshl_b32 s75, s6, 4
	v_writelane_b32 v255, s83, 24
	s_branch .Lcvp131_31
